# the two units of a workgroup run one barrier apart (unit 1 takes one extra barrier at entry, unit 0 at exit): matrix phases of one wave over the softmax of the other on each SIMD
# baseline (speedup 1.0000x reference)
.LBB0_427:
	v_or_b32_e32 v3, s3, v7
	v_lshlrev_b32_e32 v3, s1, v3
	v_add_u32_e32 v180, s42, v3
	s_movk_i32 s4, 0x1880
	v_mov_b64_e32 v[10:11], s[84:85]
	v_mad_i64_i32 v[10:11], s[4:5], v180, s4, v[10:11]
	s_lshl_b32 s4, s2, 1
	s_mov_b32 s5, 0
	v_lshl_add_u64 v[10:11], v[10:11], 0, s[4:5]
	v_lshlrev_b32_e32 v12, 4, v6
	v_mov_b32_e32 v13, 0
	v_lshl_add_u64 v[10:11], v[10:11], 0, v[12:13]
	global_load_dwordx4 v[146:149], v[10:11], off offset:96
	global_load_dwordx4 v[150:153], v[10:11], off offset:64
	global_load_dwordx4 v[154:157], v[10:11], off offset:32
	global_load_dwordx4 v[158:161], v[10:11], off
	s_lshl_b32 s81, 1, s1
	s_lshl_b32 s1, 0xffffff80, s1
	s_waitcnt vmcnt(0)
	s_add_i32 s82, s42, s1
	v_lshlrev_b32_e32 v2, 4, v2
	s_movk_i32 s1, 0x1000
	v_add3_u32 v182, v1, v2, s1
	s_movk_i32 s16, 0x1880
	v_and_b32_e32 v100, 63, v0
	v_lshrrev_b32_e32 v101, 3, v100
	v_and_b32_e32 v104, 7, v100
	v_xor_b32_e32 v104, v104, v101
	v_lshlrev_b32_e32 v104, 4, v104
	s_lshl_b32 s10, s88, 7
	s_add_u32 s10, s10, 0x800
	v_add_u32_e32 v104, s10, v104
	s_bfe_u32 s11, s75, 0x2000c
	s_and_b32 s12, s75, 0xffff0000
	s_add_u32 s12, s12, 0x8000
	s_add_u32 s13, s11, 1
	s_lshl_b32 s10, s13, 5
	v_add_u32_e32 v102, s10, v101
	v_mul_u32_u24_e32 v103, s81, v102
	v_add_u32_e32 v103, s82, v103
	s_lshl_b32 s10, s13, 12
	s_add_u32 s10, s10, s12
	s_lshl_b32 s13, s81, 3
	v_max_i32_e32 v106, 0, v103
	s_mov_b32 m0, s10
	v_mad_u32_u24 v108, v106, s16, v104
	global_load_lds_dwordx4 v108, s[84:85]
	v_add_u32_e32 v103, s13, v103
	v_max_i32_e32 v106, 0, v103
	s_add_u32 m0, s10, 0x400
	v_mad_u32_u24 v108, v106, s16, v104
	global_load_lds_dwordx4 v108, s[84:85]
	v_add_u32_e32 v103, s13, v103
	v_max_i32_e32 v106, 0, v103
	s_add_u32 m0, s10, 0x800
	v_mad_u32_u24 v108, v106, s16, v104
	global_load_lds_dwordx4 v108, s[84:85]
	v_add_u32_e32 v103, s13, v103
	v_max_i32_e32 v106, 0, v103
	s_add_u32 m0, s10, 0xc00
	v_mad_u32_u24 v108, v106, s16, v104
	global_load_lds_dwordx4 v108, s[84:85]
	s_add_u32 s13, s11, 4
	s_cmp_eq_u32 s11, 0
	s_cselect_b32 s13, 0, s13
	s_lshl_b32 s10, s13, 5
	v_add_u32_e32 v102, s10, v101
	v_mul_u32_u24_e32 v103, s81, v102
	v_add_u32_e32 v103, s82, v103
	s_lshl_b32 s10, s13, 12
	s_add_u32 s10, s10, s12
	s_lshl_b32 s13, s81, 3
	v_max_i32_e32 v106, 0, v103
	s_mov_b32 m0, s10
	v_mad_u32_u24 v108, v106, s16, v104
	global_load_lds_dwordx4 v108, s[84:85]
	v_add_u32_e32 v103, s13, v103
	v_max_i32_e32 v106, 0, v103
	s_add_u32 m0, s10, 0x400
	v_mad_u32_u24 v108, v106, s16, v104
	global_load_lds_dwordx4 v108, s[84:85]
	v_add_u32_e32 v103, s13, v103
	v_max_i32_e32 v106, 0, v103
	s_add_u32 m0, s10, 0x800
	v_mad_u32_u24 v108, v106, s16, v104
	global_load_lds_dwordx4 v108, s[84:85]
	v_add_u32_e32 v103, s13, v103
	v_max_i32_e32 v106, 0, v103
	s_add_u32 m0, s10, 0xc00
	v_mad_u32_u24 v108, v106, s16, v104
	global_load_lds_dwordx4 v108, s[84:85]
	v_and_b32_e32 v100, 63, v0
	v_lshrrev_b32_e32 v101, 3, v100
	v_and_b32_e32 v104, 7, v100
	v_lshlrev_b32_e32 v104, 4, v104
	s_lshl_b32 s10, s88, 7
	s_add_u32 s10, s10, 0x1000
	v_add_u32_e32 v104, s10, v104
	s_bfe_u32 s11, s75, 0x2000c
	s_and_b32 s12, s75, 0xffff0000
	s_add_u32 s13, s11, 1
	s_lshl_b32 s10, s13, 5
	v_add_u32_e32 v102, s10, v101
	v_mul_u32_u24_e32 v103, s81, v102
	v_add_u32_e32 v103, s82, v103
	s_lshl_b32 s10, s13, 12
	s_add_u32 s10, s10, s12
	s_lshl_b32 s13, s81, 3
	v_max_i32_e32 v106, 0, v103
	s_mov_b32 m0, s10
	v_mad_u32_u24 v108, v106, s16, v104
	global_load_lds_dwordx4 v108, s[84:85]
	v_add_u32_e32 v103, s13, v103
	v_max_i32_e32 v106, 0, v103
	s_add_u32 m0, s10, 0x400
	v_mad_u32_u24 v108, v106, s16, v104
	global_load_lds_dwordx4 v108, s[84:85]
	v_add_u32_e32 v103, s13, v103
	v_max_i32_e32 v106, 0, v103
	s_add_u32 m0, s10, 0x800
	v_mad_u32_u24 v108, v106, s16, v104
	global_load_lds_dwordx4 v108, s[84:85]
	v_add_u32_e32 v103, s13, v103
	v_max_i32_e32 v106, 0, v103
	s_add_u32 m0, s10, 0xc00
	v_mad_u32_u24 v108, v106, s16, v104
	global_load_lds_dwordx4 v108, s[84:85]
	s_add_u32 s13, s11, 4
	s_cmp_eq_u32 s11, 0
	s_cselect_b32 s13, 0, s13
	s_lshl_b32 s10, s13, 5
	v_add_u32_e32 v102, s10, v101
	v_mul_u32_u24_e32 v103, s81, v102
	v_add_u32_e32 v103, s82, v103
	s_lshl_b32 s10, s13, 12
	s_add_u32 s10, s10, s12
	s_lshl_b32 s13, s81, 3
	v_max_i32_e32 v106, 0, v103
	s_mov_b32 m0, s10
	v_mad_u32_u24 v108, v106, s16, v104
	global_load_lds_dwordx4 v108, s[84:85]
	v_add_u32_e32 v103, s13, v103
	v_max_i32_e32 v106, 0, v103
	s_add_u32 m0, s10, 0x400
	v_mad_u32_u24 v108, v106, s16, v104
	global_load_lds_dwordx4 v108, s[84:85]
	v_add_u32_e32 v103, s13, v103
	v_max_i32_e32 v106, 0, v103
	s_add_u32 m0, s10, 0x800
	v_mad_u32_u24 v108, v106, s16, v104
	global_load_lds_dwordx4 v108, s[84:85]
	v_add_u32_e32 v103, s13, v103
	v_max_i32_e32 v106, 0, v103
	s_add_u32 m0, s10, 0xc00
	v_mad_u32_u24 v108, v106, s16, v104
	global_load_lds_dwordx4 v108, s[84:85]
	s_waitcnt vmcnt(0)
	s_barrier
	v_readlane_b32 s10, v254, 14
	s_cmp_eq_u32 s10, 0
	s_cbranch_scc1 .Latt_off0
	s_barrier
